# v11 + reuse the per-CU MoE block tables built in the up phase for the down and E4 phases of the same launch (skip 4 redundant rebuilds when ph_lo shows the up phase ran)
# baseline (speedup 1.0000x reference)
; #define LAS __attribute__((address_space(3)))
; __device__ __forceinline__ void moe_tables(Frame& F, const unsigned* cnt) {
;     LAS int* tb = (LAS int*)(F.lds + TBL_OFF); LAS int* tbs = (LAS int*)(F.lds + TBL_OFF + 4096);
;     __syncthreads();
;     if (F.wave == 0) { const int c = (int)cnt[F.lane * CNT_STRIDE]; const int nb = (c + 255) >> 8; int inc = nb;
; #pragma unroll
;         for (int o = 1; o < 64; o <<= 1) { const int t = __shfl_up(inc, o); if (F.lane >= o) inc += t; }
;         const int start = inc - nb; tbs[F.lane] = start; tbs[128 + F.lane] = c; if (F.lane == 63) tbs[64] = inc;
;         for (int j = 0; j < nb; ++j) tb[start + j] = (F.lane << 16) | j; }
;     __syncthreads();
; }
.LBB0_843:
	s_cmp_lt_i32 s34, 9
	s_cselect_b64 s[0:1], -1, 0
	s_and_b64 s[2:3], s[0:1], s[2:3]
	s_andn2_b64 vcc, exec, s[2:3]
	s_cbranch_vccnz .LBB0_883
	v_mov_b32_e32 v1, v0
	s_waitcnt vmcnt(0) lgkmcnt(0)
	v_readfirstlane_b32 s2, v1
	s_cmp_gt_u32 s2, 63
	s_barrier
	s_cbranch_scc1 .LBB0_861
	s_cmp_lt_i32 s34, 8
	s_cbranch_scc1 .LBB0_861
	v_and_b32_e32 v2, 63, v1
	v_lshlrev_b32_e32 v4, 8, v2
	v_mov_b32_e32 v5, 0
	v_lshl_add_u64 v[4:5], s[36:37], 0, v[4:5]
	v_add_co_u32_e32 v4, vcc, 0x10000, v4
	v_mbcnt_lo_u32_b32 v1, -1, 0
	s_nop 0
	v_addc_co_u32_e32 v5, vcc, 0, v5, vcc
	global_load_dword v4, v[4:5], off
	v_mbcnt_hi_u32_b32 v3, -1, v1
	v_and_b32_e32 v5, 64, v3
	v_add_u32_e32 v1, -1, v3
	v_cmp_lt_i32_e32 vcc, v1, v5
	v_add_u32_e32 v6, -2, v3
	v_add_u32_e32 v7, -4, v3
	v_cndmask_b32_e32 v1, v1, v3, vcc
	v_lshlrev_b32_e32 v11, 2, v1
	v_cmp_lt_i32_e32 vcc, v6, v5
	v_add_u32_e32 v8, -8, v3
	v_add_u32_e32 v9, -16, v3
	v_cndmask_b32_e32 v6, v6, v3, vcc
	v_cmp_ne_u32_e32 vcc, 0, v2
	v_lshlrev_b32_e32 v6, 2, v6
	v_subrev_u32_e32 v10, 32, v3
	s_waitcnt vmcnt(0)
	v_add_u32_e32 v1, 0xff, v4
	v_ashrrev_i32_e32 v1, 8, v1
	ds_bpermute_b32 v11, v11, v1
	s_waitcnt lgkmcnt(0)
	v_cndmask_b32_e32 v11, 0, v11, vcc
	v_add_u32_e32 v11, v11, v1
	ds_bpermute_b32 v6, v6, v11
	v_cmp_lt_i32_e32 vcc, v7, v5
	s_nop 1
	v_cndmask_b32_e32 v7, v7, v3, vcc
	v_cmp_lt_u32_e32 vcc, 1, v2
	v_lshlrev_b32_e32 v7, 2, v7
	s_waitcnt lgkmcnt(0)
	v_cndmask_b32_e32 v6, 0, v6, vcc
	v_add_u32_e32 v6, v6, v11
	ds_bpermute_b32 v7, v7, v6
	v_cmp_lt_i32_e32 vcc, v8, v5
	s_nop 1
	v_cndmask_b32_e32 v8, v8, v3, vcc
	v_cmp_lt_u32_e32 vcc, 3, v2
	v_lshlrev_b32_e32 v8, 2, v8
	s_waitcnt lgkmcnt(0)
	v_cndmask_b32_e32 v7, 0, v7, vcc
	v_add_u32_e32 v6, v7, v6
	ds_bpermute_b32 v7, v8, v6
	v_cmp_lt_i32_e32 vcc, v9, v5
	s_nop 1
	v_cndmask_b32_e32 v8, v9, v3, vcc
	v_cmp_lt_u32_e32 vcc, 7, v2
	v_lshlrev_b32_e32 v8, 2, v8
	s_waitcnt lgkmcnt(0)
	v_cndmask_b32_e32 v7, 0, v7, vcc
	v_add_u32_e32 v6, v7, v6
	ds_bpermute_b32 v7, v8, v6
	v_cmp_lt_i32_e32 vcc, v10, v5
	s_nop 1
	v_cndmask_b32_e32 v3, v10, v3, vcc
	v_cmp_lt_u32_e32 vcc, 15, v2
	v_lshlrev_b32_e32 v3, 2, v3
	s_waitcnt lgkmcnt(0)
	v_cndmask_b32_e32 v5, 0, v7, vcc
	v_add_u32_e32 v5, v5, v6
	ds_bpermute_b32 v3, v3, v5
	v_cmp_lt_u32_e32 vcc, 31, v2
	v_lshl_add_u32 v6, v2, 2, 0
	v_add_u32_e32 v6, 0x21400, v6
	s_waitcnt lgkmcnt(0)
	v_cndmask_b32_e32 v3, 0, v3, vcc
	v_add_u32_e32 v3, v3, v5
	v_sub_u32_e32 v5, v3, v1
	v_cmp_eq_u32_e32 vcc, 63, v2
	ds_write2st64_b32 v6, v5, v4 offset1:2
	s_and_saveexec_b64 s[2:3], vcc
	s_add_i32 s4, 0, 0x21500
	v_mov_b32_e32 v4, s4
	ds_write_b32 v4, v3
	s_or_b64 exec, exec, s[2:3]
	v_cmp_lt_i32_e32 vcc, 0, v1
	s_and_saveexec_b64 s[2:3], vcc
	s_cbranch_execz .LBB0_860
	v_lshlrev_b32_e32 v4, 16, v2
	v_cmp_ne_u32_e32 vcc, 1, v1
	s_mov_b64 s[10:11], -1
	v_mov_b32_e32 v2, 0
	s_and_saveexec_b64 s[4:5], vcc
	s_cbranch_execz .LBB0_857
	v_add_u32_e32 v2, -2, v1
	v_lshrrev_b32_e32 v3, 1, v2
	v_cmp_lt_u32_e32 vcc, 13, v2
	v_mov_b32_e32 v2, 0
	v_add_u32_e32 v6, 1, v3
	s_mov_b32 s9, 0
	v_mov_b32_e32 v3, 1
	v_mov_b32_e32 v9, v2
	s_and_saveexec_b64 s[10:11], vcc
	s_cbranch_execz .LBB0_853
	v_lshl_add_u32 v2, v5, 2, 0
	v_and_b32_e32 v7, -8, v6
	v_add_u32_e32 v8, 0x20400, v2
	s_mov_b32 s15, 1
	s_mov_b64 s[12:13], 0
	s_mov_b32 s14, 0

; #define LAS __attribute__((address_space(3)))
; __device__ __forceinline__ void moe_tables(Frame& F, const unsigned* cnt) {
;     LAS int* tb = (LAS int*)(F.lds + TBL_OFF); LAS int* tbs = (LAS int*)(F.lds + TBL_OFF + 4096);
;     __syncthreads();
;     if (F.wave == 0) { const int c = (int)cnt[F.lane * CNT_STRIDE]; const int nb = (c + 255) >> 8; int inc = nb;
; #pragma unroll
;         for (int o = 1; o < 64; o <<= 1) { const int t = __shfl_up(inc, o); if (F.lane >= o) inc += t; }
;         const int start = inc - nb; tbs[F.lane] = start; tbs[128 + F.lane] = c; if (F.lane == 63) tbs[64] = inc;
;         for (int j = 0; j < nb; ++j) tb[start + j] = (F.lane << 16) | j; }
;     __syncthreads();
; }
.LBB0_937:
	s_cmp_lt_i32 s34, 10
	s_cselect_b64 s[0:1], -1, 0
	s_and_b64 s[2:3], s[0:1], s[2:3]
	s_andn2_b64 vcc, exec, s[2:3]
	s_cbranch_vccnz .LBB0_964
	v_mov_b32_e32 v1, v0
	s_waitcnt vmcnt(0) lgkmcnt(0)
	v_readfirstlane_b32 s9, v1
	v_and_b32_e32 v110, 63, v1
	s_cmp_gt_u32 s9, 63
	s_barrier
	s_cbranch_scc1 .LBB0_955
	s_cmp_lt_i32 s34, 8
	s_cbranch_scc1 .LBB0_955
	v_lshlrev_b32_e32 v2, 8, v110
	v_mov_b32_e32 v3, 0
	v_lshl_add_u64 v[2:3], s[36:37], 0, v[2:3]
	v_add_co_u32_e32 v2, vcc, 0x10000, v2
	v_mbcnt_lo_u32_b32 v1, -1, 0
	s_nop 0
	v_addc_co_u32_e32 v3, vcc, 0, v3, vcc
	global_load_dword v3, v[2:3], off
	v_mbcnt_hi_u32_b32 v2, -1, v1
	v_and_b32_e32 v4, 64, v2
	v_add_u32_e32 v1, -1, v2
	v_cmp_lt_i32_e32 vcc, v1, v4
	v_add_u32_e32 v5, -2, v2
	v_add_u32_e32 v6, -4, v2
	v_cndmask_b32_e32 v1, v1, v2, vcc
	v_lshlrev_b32_e32 v10, 2, v1
	v_cmp_lt_i32_e32 vcc, v5, v4
	v_add_u32_e32 v7, -8, v2
	v_add_u32_e32 v8, -16, v2
	v_cndmask_b32_e32 v5, v5, v2, vcc
	v_cmp_ne_u32_e32 vcc, 0, v110
	v_lshlrev_b32_e32 v5, 2, v5
	v_subrev_u32_e32 v9, 32, v2
	s_waitcnt vmcnt(0)
	v_add_u32_e32 v1, 0xff, v3
	v_ashrrev_i32_e32 v1, 8, v1
	ds_bpermute_b32 v10, v10, v1
	s_waitcnt lgkmcnt(0)
	v_cndmask_b32_e32 v10, 0, v10, vcc
	v_add_u32_e32 v10, v10, v1
	ds_bpermute_b32 v5, v5, v10
	v_cmp_lt_i32_e32 vcc, v6, v4
	s_nop 1
	v_cndmask_b32_e32 v6, v6, v2, vcc
	v_cmp_lt_u32_e32 vcc, 1, v110
	v_lshlrev_b32_e32 v6, 2, v6
	s_waitcnt lgkmcnt(0)
	v_cndmask_b32_e32 v5, 0, v5, vcc
	v_add_u32_e32 v5, v5, v10
	ds_bpermute_b32 v6, v6, v5
	v_cmp_lt_i32_e32 vcc, v7, v4
	s_nop 1
	v_cndmask_b32_e32 v7, v7, v2, vcc
	v_cmp_lt_u32_e32 vcc, 3, v110
	v_lshlrev_b32_e32 v7, 2, v7
	s_waitcnt lgkmcnt(0)
	v_cndmask_b32_e32 v6, 0, v6, vcc
	v_add_u32_e32 v5, v6, v5
	ds_bpermute_b32 v6, v7, v5
	v_cmp_lt_i32_e32 vcc, v8, v4
	s_nop 1
	v_cndmask_b32_e32 v7, v8, v2, vcc
	v_cmp_lt_u32_e32 vcc, 7, v110
	v_lshlrev_b32_e32 v7, 2, v7
	s_waitcnt lgkmcnt(0)
	v_cndmask_b32_e32 v6, 0, v6, vcc
	v_add_u32_e32 v5, v6, v5
	ds_bpermute_b32 v6, v7, v5
	v_cmp_lt_i32_e32 vcc, v9, v4
	s_nop 1
	v_cndmask_b32_e32 v2, v9, v2, vcc
	v_cmp_lt_u32_e32 vcc, 15, v110
	v_lshlrev_b32_e32 v2, 2, v2
	s_waitcnt lgkmcnt(0)
	v_cndmask_b32_e32 v4, 0, v6, vcc
	v_add_u32_e32 v4, v4, v5
	ds_bpermute_b32 v2, v2, v4
	v_cmp_lt_u32_e32 vcc, 31, v110
	v_lshl_add_u32 v5, v110, 2, 0
	v_add_u32_e32 v6, 0x21400, v5
	s_waitcnt lgkmcnt(0)
	v_cndmask_b32_e32 v2, 0, v2, vcc
	v_add_u32_e32 v2, v2, v4
	v_sub_u32_e32 v5, v2, v1
	v_cmp_eq_u32_e32 vcc, 63, v110
	ds_write2st64_b32 v6, v5, v3 offset1:2
	s_and_saveexec_b64 s[2:3], vcc
	s_add_i32 s4, 0, 0x21500
	v_mov_b32_e32 v3, s4
	ds_write_b32 v3, v2
	s_or_b64 exec, exec, s[2:3]
	v_cmp_lt_i32_e32 vcc, 0, v1
	s_and_saveexec_b64 s[2:3], vcc
	s_cbranch_execz .LBB0_954
	v_lshlrev_b32_e32 v4, 16, v110
	v_cmp_ne_u32_e32 vcc, 1, v1
	s_mov_b64 s[10:11], -1
	v_mov_b32_e32 v2, 0
	s_and_saveexec_b64 s[4:5], vcc
	s_cbranch_execz .LBB0_951
	v_add_u32_e32 v2, -2, v1
	v_lshrrev_b32_e32 v3, 1, v2
	v_cmp_lt_u32_e32 vcc, 13, v2
	v_mov_b32_e32 v2, 0
	v_add_u32_e32 v6, 1, v3
	s_mov_b32 s16, 0
	v_mov_b32_e32 v3, 1
	v_mov_b32_e32 v9, v2
	s_and_saveexec_b64 s[10:11], vcc
	s_cbranch_execz .LBB0_947
	v_lshl_add_u32 v2, v5, 2, 0
	v_and_b32_e32 v7, -8, v6
	v_add_u32_e32 v8, 0x20400, v2
	s_mov_b32 s15, 1
	s_mov_b64 s[12:13], 0
	s_mov_b32 s14, 0

; #define LAS __attribute__((address_space(3)))
; __device__ __forceinline__ void moe_tables(Frame& F, const unsigned* cnt) {
;     LAS int* tb = (LAS int*)(F.lds + TBL_OFF); LAS int* tbs = (LAS int*)(F.lds + TBL_OFF + 4096);
;     __syncthreads();
;     if (F.wave == 0) { const int c = (int)cnt[F.lane * CNT_STRIDE]; const int nb = (c + 255) >> 8; int inc = nb;
; #pragma unroll
;         for (int o = 1; o < 64; o <<= 1) { const int t = __shfl_up(inc, o); if (F.lane >= o) inc += t; }
;         const int start = inc - nb; tbs[F.lane] = start; tbs[128 + F.lane] = c; if (F.lane == 63) tbs[64] = inc;
;         for (int j = 0; j < nb; ++j) tb[start + j] = (F.lane << 16) | j; }
;     __syncthreads();
; }
.LBB0_1695:
	s_cmp_lt_i32 s34, 18
	s_cselect_b64 s[0:1], -1, 0
	s_and_b64 s[2:3], s[0:1], s[2:3]
	s_andn2_b64 vcc, exec, s[2:3]
	s_cbranch_vccnz .LBB0_1735
	v_mov_b32_e32 v1, v0
	s_waitcnt vmcnt(0) lgkmcnt(0)
	v_readfirstlane_b32 s2, v1
	s_cmp_gt_u32 s2, 63
	s_barrier
	s_cbranch_scc1 .LBB0_1713
	s_cmp_lt_i32 s34, 17
	s_cbranch_scc1 .LBB0_1713
	v_and_b32_e32 v2, 63, v1
	v_lshlrev_b32_e32 v4, 8, v2
	v_mov_b32_e32 v5, 0
	v_lshl_add_u64 v[4:5], s[36:37], 0, v[4:5]
	v_add_co_u32_e32 v4, vcc, 0x14000, v4
	v_mbcnt_hi_u32_b32 v3, -1, v230
	s_nop 0
	v_addc_co_u32_e32 v5, vcc, 0, v5, vcc
	global_load_dword v4, v[4:5], off
	v_and_b32_e32 v5, 64, v3
	v_add_u32_e32 v1, -1, v3
	v_cmp_lt_i32_e32 vcc, v1, v5
	v_add_u32_e32 v6, -2, v3
	v_add_u32_e32 v7, -4, v3
	v_cndmask_b32_e32 v1, v1, v3, vcc
	v_lshlrev_b32_e32 v11, 2, v1
	v_cmp_lt_i32_e32 vcc, v6, v5
	v_add_u32_e32 v8, -8, v3
	v_add_u32_e32 v9, -16, v3
	v_cndmask_b32_e32 v6, v6, v3, vcc
	v_cmp_ne_u32_e32 vcc, 0, v2
	v_lshlrev_b32_e32 v6, 2, v6
	v_subrev_u32_e32 v10, 32, v3
	s_waitcnt vmcnt(0)
	v_add_u32_e32 v1, 0xff, v4
	v_ashrrev_i32_e32 v1, 8, v1
	ds_bpermute_b32 v11, v11, v1
	s_waitcnt lgkmcnt(0)
	v_cndmask_b32_e32 v11, 0, v11, vcc
	v_add_u32_e32 v11, v11, v1
	ds_bpermute_b32 v6, v6, v11
	v_cmp_lt_i32_e32 vcc, v7, v5
	s_nop 1
	v_cndmask_b32_e32 v7, v7, v3, vcc
	v_cmp_lt_u32_e32 vcc, 1, v2
	v_lshlrev_b32_e32 v7, 2, v7
	s_waitcnt lgkmcnt(0)
	v_cndmask_b32_e32 v6, 0, v6, vcc
	v_add_u32_e32 v6, v6, v11
	ds_bpermute_b32 v7, v7, v6
	v_cmp_lt_i32_e32 vcc, v8, v5
	s_nop 1
	v_cndmask_b32_e32 v8, v8, v3, vcc
	v_cmp_lt_u32_e32 vcc, 3, v2
	v_lshlrev_b32_e32 v8, 2, v8
	s_waitcnt lgkmcnt(0)
	v_cndmask_b32_e32 v7, 0, v7, vcc
	v_add_u32_e32 v6, v7, v6
	ds_bpermute_b32 v7, v8, v6
	v_cmp_lt_i32_e32 vcc, v9, v5
	s_nop 1
	v_cndmask_b32_e32 v8, v9, v3, vcc
	v_cmp_lt_u32_e32 vcc, 7, v2
	v_lshlrev_b32_e32 v8, 2, v8
	s_waitcnt lgkmcnt(0)
	v_cndmask_b32_e32 v7, 0, v7, vcc
	v_add_u32_e32 v6, v7, v6
	ds_bpermute_b32 v7, v8, v6
	v_cmp_lt_i32_e32 vcc, v10, v5
	s_nop 1
	v_cndmask_b32_e32 v3, v10, v3, vcc
	v_cmp_lt_u32_e32 vcc, 15, v2
	v_lshlrev_b32_e32 v3, 2, v3
	s_waitcnt lgkmcnt(0)
	v_cndmask_b32_e32 v5, 0, v7, vcc
	v_add_u32_e32 v5, v5, v6
	ds_bpermute_b32 v3, v3, v5
	v_cmp_lt_u32_e32 vcc, 31, v2
	v_lshl_add_u32 v6, v2, 2, 0
	v_add_u32_e32 v6, 0x21400, v6
	s_waitcnt lgkmcnt(0)
	v_cndmask_b32_e32 v3, 0, v3, vcc
	v_add_u32_e32 v3, v3, v5
	v_sub_u32_e32 v5, v3, v1
	v_cmp_eq_u32_e32 vcc, 63, v2
	ds_write2st64_b32 v6, v5, v4 offset1:2
	s_and_saveexec_b64 s[2:3], vcc
	s_add_i32 s4, 0, 0x21500
	v_mov_b32_e32 v4, s4
	ds_write_b32 v4, v3
	s_or_b64 exec, exec, s[2:3]
	v_cmp_lt_i32_e32 vcc, 0, v1
	s_and_saveexec_b64 s[2:3], vcc
	s_cbranch_execz .LBB0_1712
	v_lshlrev_b32_e32 v4, 16, v2
	v_cmp_ne_u32_e32 vcc, 1, v1
	s_mov_b64 s[8:9], -1
	v_mov_b32_e32 v2, 0
	s_and_saveexec_b64 s[4:5], vcc
	s_cbranch_execz .LBB0_1709
	v_add_u32_e32 v2, -2, v1
	v_lshrrev_b32_e32 v3, 1, v2
	v_cmp_lt_u32_e32 vcc, 13, v2
	v_mov_b32_e32 v2, 0
	v_add_u32_e32 v6, 1, v3
	s_mov_b32 s14, 0
	v_mov_b32_e32 v3, 1
	v_mov_b32_e32 v9, v2
	s_and_saveexec_b64 s[8:9], vcc
	s_cbranch_execz .LBB0_1705
	v_lshl_add_u32 v2, v5, 2, 0
	v_and_b32_e32 v7, -8, v6
	v_add_u32_e32 v8, 0x20400, v2
	s_mov_b32 s13, 1
	s_mov_b64 s[10:11], 0
	s_mov_b32 s12, 0

; #define LAS __attribute__((address_space(3)))
; __device__ __forceinline__ void moe_tables(Frame& F, const unsigned* cnt) {
;     LAS int* tb = (LAS int*)(F.lds + TBL_OFF); LAS int* tbs = (LAS int*)(F.lds + TBL_OFF + 4096);
;     __syncthreads();
;     if (F.wave == 0) { const int c = (int)cnt[F.lane * CNT_STRIDE]; const int nb = (c + 255) >> 8; int inc = nb;
; #pragma unroll
;         for (int o = 1; o < 64; o <<= 1) { const int t = __shfl_up(inc, o); if (F.lane >= o) inc += t; }
;         const int start = inc - nb; tbs[F.lane] = start; tbs[128 + F.lane] = c; if (F.lane == 63) tbs[64] = inc;
;         for (int j = 0; j < nb; ++j) tb[start + j] = (F.lane << 16) | j; }
;     __syncthreads();
; }
.LBB0_1789:
	s_cmp_lt_i32 s34, 19
	s_cselect_b64 s[0:1], -1, 0
	s_and_b64 s[2:3], s[0:1], s[2:3]
	s_andn2_b64 vcc, exec, s[2:3]
	s_cbranch_vccnz .LBB0_1812
	s_waitcnt vmcnt(0) lgkmcnt(0)
	v_readfirstlane_b32 s14, v0
	v_and_b32_e32 v24, 63, v0
	s_cmp_gt_u32 s14, 63
	s_barrier
	s_cbranch_scc1 .LBB0_1807
	s_cmp_lt_i32 s34, 17
	s_cbranch_scc1 .LBB0_1807
	v_lshlrev_b32_e32 v0, 8, v24
	v_mov_b32_e32 v1, 0
	v_lshl_add_u64 v[0:1], s[36:37], 0, v[0:1]
	v_add_co_u32_e32 v0, vcc, 0x14000, v0
	s_nop 1
	v_addc_co_u32_e32 v1, vcc, 0, v1, vcc
	global_load_dword v1, v[0:1], off
	v_mbcnt_hi_u32_b32 v0, -1, v230
	v_and_b32_e32 v3, 64, v0
	v_add_u32_e32 v2, -1, v0
	v_cmp_lt_i32_e32 vcc, v2, v3
	v_add_u32_e32 v4, -2, v0
	v_add_u32_e32 v5, -4, v0
	v_cndmask_b32_e32 v2, v2, v0, vcc
	v_lshlrev_b32_e32 v9, 2, v2
	v_cmp_lt_i32_e32 vcc, v4, v3
	v_add_u32_e32 v6, -8, v0
	v_add_u32_e32 v7, -16, v0
	v_cndmask_b32_e32 v4, v4, v0, vcc
	v_cmp_ne_u32_e32 vcc, 0, v24
	v_lshlrev_b32_e32 v4, 2, v4
	v_subrev_u32_e32 v8, 32, v0
	s_waitcnt vmcnt(0)
	v_add_u32_e32 v2, 0xff, v1
	v_ashrrev_i32_e32 v2, 8, v2
	ds_bpermute_b32 v9, v9, v2
	s_waitcnt lgkmcnt(0)
	v_cndmask_b32_e32 v9, 0, v9, vcc
	v_add_u32_e32 v9, v9, v2
	ds_bpermute_b32 v4, v4, v9
	v_cmp_lt_i32_e32 vcc, v5, v3
	s_nop 1
	v_cndmask_b32_e32 v5, v5, v0, vcc
	v_cmp_lt_u32_e32 vcc, 1, v24
	v_lshlrev_b32_e32 v5, 2, v5
	s_waitcnt lgkmcnt(0)
	v_cndmask_b32_e32 v4, 0, v4, vcc
	v_add_u32_e32 v4, v4, v9
	ds_bpermute_b32 v5, v5, v4
	v_cmp_lt_i32_e32 vcc, v6, v3
	s_nop 1
	v_cndmask_b32_e32 v6, v6, v0, vcc
	v_cmp_lt_u32_e32 vcc, 3, v24
	v_lshlrev_b32_e32 v6, 2, v6
	s_waitcnt lgkmcnt(0)
	v_cndmask_b32_e32 v5, 0, v5, vcc
	v_add_u32_e32 v4, v5, v4
	ds_bpermute_b32 v5, v6, v4
	v_cmp_lt_i32_e32 vcc, v7, v3
	s_nop 1
	v_cndmask_b32_e32 v6, v7, v0, vcc
	v_cmp_lt_u32_e32 vcc, 7, v24
	v_lshlrev_b32_e32 v6, 2, v6
	s_waitcnt lgkmcnt(0)
	v_cndmask_b32_e32 v5, 0, v5, vcc
	v_add_u32_e32 v4, v5, v4
	ds_bpermute_b32 v5, v6, v4
	v_cmp_lt_i32_e32 vcc, v8, v3
	s_nop 1
	v_cndmask_b32_e32 v0, v8, v0, vcc
	v_cmp_lt_u32_e32 vcc, 15, v24
	v_lshlrev_b32_e32 v0, 2, v0
	s_waitcnt lgkmcnt(0)
	v_cndmask_b32_e32 v3, 0, v5, vcc
	v_add_u32_e32 v3, v3, v4
	ds_bpermute_b32 v0, v0, v3
	v_cmp_lt_u32_e32 vcc, 31, v24
	v_lshl_add_u32 v4, v24, 2, 0
	v_add_u32_e32 v5, 0x21400, v4
	s_waitcnt lgkmcnt(0)
	v_cndmask_b32_e32 v0, 0, v0, vcc
	v_add_u32_e32 v0, v0, v3
	v_sub_u32_e32 v4, v0, v2
	v_cmp_eq_u32_e32 vcc, 63, v24
	ds_write2st64_b32 v5, v4, v1 offset1:2
	s_and_saveexec_b64 s[2:3], vcc
	s_add_i32 s4, 0, 0x21500
	v_mov_b32_e32 v1, s4
	ds_write_b32 v1, v0
	s_or_b64 exec, exec, s[2:3]
	v_cmp_lt_i32_e32 vcc, 0, v2
	s_and_saveexec_b64 s[2:3], vcc
	s_cbranch_execz .LBB0_1806
	v_lshlrev_b32_e32 v3, 16, v24
	v_cmp_ne_u32_e32 vcc, 1, v2
	s_mov_b64 s[8:9], -1
	v_mov_b32_e32 v0, 0
	s_and_saveexec_b64 s[4:5], vcc
	s_cbranch_execz .LBB0_1803
	v_add_u32_e32 v0, -2, v2
	v_lshrrev_b32_e32 v1, 1, v0
	v_cmp_lt_u32_e32 vcc, 13, v0
	v_mov_b32_e32 v0, 0
	v_add_u32_e32 v5, 1, v1
	s_mov_b32 s15, 0
	v_mov_b32_e32 v1, 1
	v_mov_b32_e32 v8, v0
	s_and_saveexec_b64 s[8:9], vcc
	s_cbranch_execz .LBB0_1799
	v_lshl_add_u32 v0, v4, 2, 0
	v_and_b32_e32 v6, -8, v5
	v_add_u32_e32 v7, 0x20400, v0
	s_mov_b32 s13, 1
	s_mov_b64 s[10:11], 0
	s_mov_b32 s12, 0
